# k_point: Wk LDS images at 152-B row stride (bank-conflict-free for the mod-32 ds_read2_b64 fragment reads), s=2 fragment reads as four ds_read_b64, waits recounted
# speedup vs baseline: 1.0024x; 1.0024x over previous
.LBB0_20:
	s_or_b64 exec, exec, s[4:5]
	s_waitcnt vmcnt(5)
	v_cvt_pk_f16_f32 v1, v24, v25
	v_cvt_pk_f16_f32 v0, v22, v23
	v_add_u32_e32 v135, 0xfffffc00, v106
	v_mul_u32_u24_e32 v136, 0xe39, v135
	v_add_u32_e32 v137, 0x200, v135
	v_lshrrev_b32_e32 v136, 16, v136
	v_mul_u32_u24_e32 v138, 0xe39, v137
	v_add_lshl_u32 v136, v136, v135, 3
	v_lshrrev_b32_e32 v138, 16, v138
	v_add_lshl_u32 v137, v138, v137, 3
	v_mul_u32_u24_e32 v138, 0xe39, v106
	v_lshrrev_b32_e32 v138, 16, v138
	v_add_lshl_u32 v138, v138, v106, 3
	ds_write_b64 v136, v[0:1] offset:46080
	s_waitcnt vmcnt(4)
	v_cvt_pk_f16_f32 v1, v20, v21
	v_cvt_pk_f16_f32 v0, v18, v19
	ds_write_b64 v137, v[0:1] offset:46080
	s_and_saveexec_b64 s[4:5], s[2:3]
	s_cbranch_execz .LBB0_22
	v_mul_u32_u24_e32 v18, 0xe39, v106
	s_movk_i32 s6, 0xffee
	v_mul_i32_i24_sdwa v19, v18, s6 dst_sel:DWORD dst_unused:UNUSED_PAD src0_sel:WORD_1 src1_sel:DWORD
	s_movk_i32 s6, 0xa0
	s_waitcnt vmcnt(3)
	v_cvt_pk_f16_f32 v0, v14, v15
	v_mul_u32_u24_sdwa v14, v18, s6 dst_sel:DWORD dst_unused:UNUSED_PAD src0_sel:WORD_1 src1_sel:DWORD
	v_add_lshl_u32 v15, v19, v106, 3
	v_cvt_pk_f16_f32 v1, v16, v17
	v_add3_u32 v14, 0, v14, v15
	ds_write_b64 v138, v[0:1] offset:46080
.LBB0_22:
	s_or_b64 exec, exec, s[4:5]
	s_waitcnt vmcnt(2)
	v_cvt_pk_f16_f32 v1, v12, v13
	v_cvt_pk_f16_f32 v0, v10, v11
	ds_write_b64 v136, v[0:1] offset:57600
	s_waitcnt vmcnt(1)
	v_cvt_pk_f16_f32 v1, v8, v9
	v_cvt_pk_f16_f32 v0, v6, v7
	ds_write_b64 v137, v[0:1] offset:57600
	s_and_saveexec_b64 s[0:1], s[2:3]
	s_cbranch_execz .LBB0_24
	v_mul_u32_u24_e32 v6, 0xe39, v106
	s_movk_i32 s2, 0xffee
	v_mul_i32_i24_sdwa v7, v6, s2 dst_sel:DWORD dst_unused:UNUSED_PAD src0_sel:WORD_1 src1_sel:DWORD
	s_movk_i32 s2, 0xa0
	s_waitcnt vmcnt(0)
	v_cvt_pk_f16_f32 v0, v2, v3
	v_mul_u32_u24_sdwa v2, v6, s2 dst_sel:DWORD dst_unused:UNUSED_PAD src0_sel:WORD_1 src1_sel:DWORD
	v_add_lshl_u32 v3, v7, v106, 3
	v_cvt_pk_f16_f32 v1, v4, v5
	v_add3_u32 v2, 0, v2, v3
	ds_write_b64 v138, v[0:1] offset:57600

.LBB0_26:
	s_or_b64 exec, exec, s[2:3]
	v_or_b32_e32 v0, 2, v104
	s_movk_i32 s0, 0x2d00
	v_mad_u32_u24 v28, v0, s0, 0
	v_mul_u32_u24_e32 v0, 0x140, v0
	v_lshlrev_b32_e32 v1, 2, v93
	v_add_u32_e32 v30, v28, v88
	v_add3_u32 v29, s11, v0, v1
	v_add3_u32 v32, v28, v92, v88
	v_add_u32_e32 v33, v30, v92
	s_waitcnt vmcnt(0)
	ds_read_b128 v[0:3], v29
	ds_read_b64_tr_b16 v[4:5], v32
	ds_read_b64_tr_b16 v[6:7], v33 offset:2560
	v_mov_b32_e32 v62, v52
	ds_read_b64_tr_b16 v[8:9], v32 offset:32
	v_lshl_add_u32 v31, v91, 1, v28
	s_waitcnt lgkmcnt(1)
	v_mfma_f32_16x16x32_f16 v[4:7], v[4:7], v[62:65], v[0:3]
	ds_read_b64_tr_b16 v[10:11], v33 offset:2592
	ds_read_b64_tr_b16 v[12:13], v32 offset:5120
	ds_read_b64_tr_b16 v[14:15], v33 offset:7680
	v_add_u32_e32 v34, v31, v92
	ds_read_b64_tr_b16 v[0:1], v34 offset:10240
	v_mov_b32_e32 v2, 0
	v_mov_b32_e32 v3, v2
	s_waitcnt lgkmcnt(1)
	v_mfma_f32_16x16x32_f16 v[4:7], v[12:15], v[58:61], v[4:7]
	ds_read_b64_tr_b16 v[12:13], v34 offset:10272
	ds_read_b128 v[16:19], v29 offset:64
	v_mov_b32_e32 v14, v2
	s_waitcnt lgkmcnt(2)
	v_mfma_f32_16x16x32_f16 v[4:7], v[0:3], v[54:57], v[4:7]
	ds_read_b64_tr_b16 v[20:21], v32 offset:5152
	ds_read_b64_tr_b16 v[22:23], v33 offset:7712
	v_mov_b32_e32 v15, v2
	s_waitcnt lgkmcnt(2)
	v_mfma_f32_16x16x32_f16 v[8:11], v[8:11], v[62:65], v[16:19]
	ds_read_b64_tr_b16 v[24:25], v32 offset:64
	v_add3_u32 v28, v28, v95, v88
	v_add_u32_e32 v30, v30, v95
	ds_read_b128 v[16:19], v29 offset:128
	s_waitcnt lgkmcnt(2)
	v_mfma_f32_16x16x32_f16 v[8:11], v[20:23], v[58:61], v[8:11]
	ds_read_b64_tr_b16 v[26:27], v33 offset:2624
	ds_read_b64_tr_b16 v[20:21], v32 offset:5184
	s_movk_i32 s2, 0x98
	v_mfma_f32_16x16x32_f16 v[8:11], v[12:15], v[54:57], v[8:11]
	ds_read_b64_tr_b16 v[22:23], v33 offset:7744
	ds_read_b64_tr_b16 v[0:1], v34 offset:10304
	v_mad_u32_u24 v35, v102, s2, v86
	s_waitcnt lgkmcnt(3)
	v_mfma_f32_16x16x32_f16 v[12:15], v[24:27], v[62:65], v[16:19]
	ds_read_b64_tr_b16 v[24:25], v28
	s_nop 1
	ds_read_b128 v[16:19], v29 offset:192
	v_add_u32_e32 v49, v35, v50
	s_waitcnt lgkmcnt(3)
	v_mfma_f32_16x16x32_f16 v[12:15], v[20:23], v[58:61], v[12:15]
	ds_read_b64_tr_b16 v[26:27], v30 offset:2560
	ds_read_b64_tr_b16 v[20:21], v28 offset:5120
	v_lshlrev_b32_e32 v48, 1, v87
	s_waitcnt lgkmcnt(4)
	v_mfma_f32_16x16x32_f16 v[12:15], v[0:3], v[54:57], v[12:15]
	ds_read_b64_tr_b16 v[22:23], v30 offset:7680
	v_add_u32_e32 v0, v31, v95
	ds_read_b64_tr_b16 v[0:1], v0 offset:10240
	s_waitcnt lgkmcnt(3)
	v_mfma_f32_16x16x32_f16 v[16:19], v[24:27], v[62:65], v[16:19]
	ds_read_b128 v[24:27], v29 offset:256
	ds_read_b64_tr_b16 v[28:29], v32 offset:128
	v_add_u32_e32 v36, v35, v48
	s_waitcnt lgkmcnt(3)
	v_mfma_f32_16x16x32_f16 v[16:19], v[20:23], v[58:61], v[16:19]
	ds_read_b64_tr_b16 v[30:31], v33 offset:2688
	ds_read_b64_tr_b16 v[20:21], v32 offset:5248
	v_add_u32_e32 v32, 0xb000, v49
	s_waitcnt lgkmcnt(4)
	v_mfma_f32_16x16x32_f16 v[16:19], v[0:3], v[54:57], v[16:19]
	ds_read_b64_tr_b16 v[22:23], v33 offset:7808
	ds_read_b64_tr_b16 v[0:1], v34 offset:10368
	v_add_u32_e32 v44, 0x80, v36
	s_waitcnt lgkmcnt(3)
	v_mfma_f32_16x16x32_f16 v[24:27], v[28:31], v[62:65], v[24:27]
	ds_read2_b64 v[28:31], v32 offset0:128 offset1:132
	ds_read2_b64 v[32:35], v32 offset0:136 offset1:140
	v_add_u32_e32 v40, 0xb800, v49
	s_waitcnt lgkmcnt(3)
	v_mfma_f32_16x16x32_f16 v[20:23], v[20:23], v[58:61], v[24:27]
	ds_read2_b64 v[36:39], v40 offset0:176 offset1:180
	v_cmp_gt_u32_e64 s[0:1], 32, v103
	v_cvt_pk_f16_f32 v11, v10, v11
	ds_read_b64 v[126:127], v44 offset:46080
	ds_read_b64 v[128:129], v44 offset:50944
	s_waitcnt lgkmcnt(4)
	v_mfma_f32_16x16x32_f16 v[20:23], v[0:3], v[54:57], v[20:23]
	v_cvt_pk_f16_f32 v10, v8, v9
	v_cvt_pk_f16_f32 v9, v6, v7
	v_cvt_pk_f16_f32 v8, v4, v5
	ds_read2_b64 v[4:7], v40 offset0:184 offset1:188
	v_cvt_pk_f16_f32 v19, v18, v19
	s_nop 2
	v_cvt_pk_f16_f32 v0, v22, v23
	v_cvt_pk_f16_f32 v1, v20, v21
	v_cndmask_b32_e64 v21, 0, v0, s[0:1]
	v_add_u32_e32 v0, 0xc700, v49
	ds_read2_b64 v[40:43], v0 offset1:4
	s_waitcnt lgkmcnt(6)
	v_mfma_f32_16x16x32_f16 v[28:31], v[28:31], v[8:11], 0
	v_cndmask_b32_e64 v20, 0, v1, s[0:1]
	v_cvt_pk_f16_f32 v18, v16, v17
	v_cvt_pk_f16_f32 v17, v14, v15
	v_cvt_pk_f16_f32 v16, v12, v13
	ds_read2_b64 v[12:15], v0 offset0:8 offset1:12
	s_waitcnt lgkmcnt(4)
	v_mov_b32_e32 v0, v126
	v_mov_b32_e32 v1, v127
	ds_read_b64 v[130:131], v44 offset:48512
	ds_read_b64 v[132:133], v44 offset:53376
	v_mfma_f32_16x16x32_f16 v[28:31], v[32:35], v[16:19], v[28:31]
	v_mov_b32_e32 v22, v2
	v_mov_b32_e32 v23, v2
	v_add_u32_e32 v24, 0xcf00, v49
	ds_read2_b64 v[32:35], v24 offset0:48 offset1:52
	ds_read2_b64 v[52:55], v24 offset0:56 offset1:60
	v_mfma_f32_16x16x32_f16 v[28:31], v[0:3], v[20:23], v[28:31]
	v_or_b32_e32 v0, 64, v102
	v_min_u32_e32 v0, 0x47, v0
	v_mad_u32_u24 v49, v0, s2, v86
	v_add_u32_e32 v0, v49, v50
	v_add_u32_e32 v0, 0xb000, v0
	ds_read2_b64 v[56:59], v0 offset0:128 offset1:132
	ds_read2_b64 v[60:63], v0 offset0:136 offset1:140
	v_mfma_f32_16x16x32_f16 v[36:39], v[36:39], v[8:11], 0
	s_waitcnt lgkmcnt(5)
	v_mov_b32_e32 v0, v130
	v_mov_b32_e32 v1, v131
	s_movk_i32 s2, 0x48
	s_waitcnt lgkmcnt(7)
	v_mfma_f32_16x16x32_f16 v[4:7], v[4:7], v[16:19], v[36:39]
	v_mov_b32_e32 v51, v2
	v_mfma_f32_16x16x32_f16 v[24:27], v[0:3], v[20:23], v[4:7]
	s_waitcnt lgkmcnt(4)
	v_mov_b32_e32 v0, v128
	v_mov_b32_e32 v1, v129
	v_mfma_f32_16x16x32_f16 v[4:7], v[40:43], v[8:11], 0
	v_mfma_f32_16x16x32_f16 v[4:7], v[12:15], v[16:19], v[4:7]
	v_mfma_f32_16x16x32_f16 v[12:15], v[0:3], v[20:23], v[4:7]
	v_mov_b32_e32 v0, v132
	v_mov_b32_e32 v1, v133
	s_waitcnt lgkmcnt(3)
	v_mfma_f32_16x16x32_f16 v[4:7], v[32:35], v[8:11], 0
	s_waitcnt lgkmcnt(2)
	v_mfma_f32_16x16x32_f16 v[4:7], v[52:55], v[16:19], v[4:7]
	v_mfma_f32_16x16x32_f16 v[32:35], v[0:3], v[20:23], v[4:7]
	v_add_u32_e32 v0, v49, v48
	ds_read_b64 v[0:1], v0 offset:46208
	s_waitcnt lgkmcnt(2)
	v_mfma_f32_16x16x32_f16 v[4:7], v[56:59], v[8:11], 0
	v_mul_lo_u32 v8, v97, s2
	s_mov_b32 s2, 0x3e2e1a92
	v_ashrrev_i32_e32 v9, 31, v8
	s_waitcnt lgkmcnt(1)
	v_mfma_f32_16x16x32_f16 v[4:7], v[60:63], v[16:19], v[4:7]
	s_waitcnt lgkmcnt(0)
	v_mfma_f32_16x16x32_f16 v[4:7], v[0:3], v[20:23], v[4:7]
	v_mov_b32_e32 v0, s63
	v_mov_b32_e32 v1, s61
	v_cndmask_b32_e32 v1, v0, v1, vcc
	v_mov_b32_e32 v0, s62
	v_mov_b32_e32 v3, s60
	v_cndmask_b32_e32 v0, v0, v3, vcc
	v_mov_b32_e32 v2, v29
	v_mov_b32_e32 v3, v30
	v_pk_mul_f32 v[2:3], v[2:3], s[2:3] op_sel_hi:[1,0]
	v_lshl_add_u64 v[0:1], v[8:9], 1, v[0:1]
	v_fma_mixlo_f16 v8, v28, s2, 0
	v_cvt_pk_f16_f32 v3, v2, v3
	v_pack_b32_f16 v2, v8, v3
	v_fma_mixlo_f16 v8, v31, s2, 0
	v_lshl_add_u64 v[0:1], v[0:1], 0, v[50:51]
	v_alignbit_b32 v3, v8, v3, 16
	global_store_dwordx2 v[0:1], v[2:3], off
	v_mov_b32_e32 v2, v25
	v_mov_b32_e32 v3, v26
	v_pk_mul_f32 v[2:3], v[2:3], s[2:3] op_sel_hi:[1,0]
	v_fma_mixlo_f16 v8, v24, s2, 0
	v_cvt_pk_f16_f32 v3, v2, v3
	v_pack_b32_f16 v2, v8, v3
	v_fma_mixlo_f16 v8, v27, s2, 0
	v_alignbit_b32 v3, v8, v3, 16
	global_store_dwordx2 v[0:1], v[2:3], off offset:32
	v_mov_b32_e32 v2, v13
	v_mov_b32_e32 v3, v14
	v_pk_mul_f32 v[2:3], v[2:3], s[2:3] op_sel_hi:[1,0]
	v_fma_mixlo_f16 v8, v12, s2, 0
	v_cvt_pk_f16_f32 v3, v2, v3
	v_pack_b32_f16 v2, v8, v3
	v_fma_mixlo_f16 v8, v15, s2, 0
	v_alignbit_b32 v3, v8, v3, 16
	global_store_dwordx2 v[0:1], v[2:3], off offset:64
	v_mov_b32_e32 v2, v33
	v_mov_b32_e32 v3, v34
	v_pk_mul_f32 v[2:3], v[2:3], s[2:3] op_sel_hi:[1,0]
	v_fma_mixlo_f16 v8, v32, s2, 0
	v_cvt_pk_f16_f32 v3, v2, v3
	v_pack_b32_f16 v2, v8, v3
	v_fma_mixlo_f16 v8, v35, s2, 0
	v_alignbit_b32 v3, v8, v3, 16
	global_store_dwordx2 v[0:1], v[2:3], off offset:96
	s_and_saveexec_b64 s[4:5], s[0:1]
	s_cbranch_execz .LBB0_28
	v_mov_b32_e32 v2, v5
	v_mov_b32_e32 v3, v6
	v_pk_mul_f32 v[2:3], v[2:3], s[2:3] op_sel_hi:[1,0]
	v_fma_mixlo_f16 v4, v4, s2, 0
	v_cvt_pk_f16_f32 v3, v2, v3
	v_pack_b32_f16 v2, v4, v3
	v_fma_mixlo_f16 v4, v7, s2, 0
	v_alignbit_b32 v3, v4, v3, 16
	global_store_dwordx2 v[0:1], v[2:3], off offset:128
